# speedup vs baseline: 1.0102x; 1.0040x over previous
.LBB0_21:
	v_exp_f32_e64 v156, -|v154|
	v_max_f32 v157, 0, v154
	v_add_f32 v156, 1.0, v156
	v_log_f32 v156, v156
	s_nop 0
	v_fma_mixlo_f16 v155, v156, 1.0, v157
	ds_write_b16 v148, v155
	v_mov_b32_e32 v192, v106
	v_mov_b32_e32 v193, v110
	v_mul_f32 v182, -2.0, v153
	s_nop 6
	ds_read_b128 v[208:211], v139
	s_waitcnt lgkmcnt(1)
	s_barrier
	ds_read_b128 v[212:215], v140
	ds_read_b128 v[216:219], v141
	s_waitcnt lgkmcnt(2)
	v_smfmac_f32_16x16x64_f16 v[192:195], v[208:211], v[6:13], v191
	ds_read_b128 v[220:223], v142
	s_waitcnt lgkmcnt(2)
	v_smfmac_f32_16x16x64_f16 v[192:195], v[212:215], v[14:21], v191
	s_waitcnt lgkmcnt(1)
	v_smfmac_f32_16x16x64_f16 v[192:195], v[216:219], v[26:33], v191
	s_waitcnt lgkmcnt(0)
	v_smfmac_f32_16x16x64_f16 v[192:195], v[220:223], v[34:41], v191
	s_nop 7
	v_cndmask_b32_e64 v154, v192, v193, s[0:1]
	v_exp_f32_e64 v156, -|v154|
	v_max_f32 v157, 0, v154
	v_add_f32 v156, 1.0, v156
	v_log_f32 v156, v156
	s_nop 0
	v_fma_mixlo_f16 v155, v156, 1.0, v157
	ds_write_b16 v149, v155
	v_mov_b32_e32 v200, v114
	v_mov_b32_e32 v201, v118
	v_mov_b32_e32 v204, v122
	v_mov_b32_e32 v205, v126
	s_nop 3
	ds_read_b128 v[208:211], v143
	s_waitcnt lgkmcnt(1)
	s_barrier
	ds_read_b128 v[212:215], v144
	ds_read_b128 v[216:219], v145
	s_waitcnt lgkmcnt(2)
	v_smfmac_f32_16x16x64_f16 v[200:203], v[208:211], v[42:49], v191
	ds_read_b128 v[220:223], v146
	v_smfmac_f32_16x16x64_f16 v[204:207], v[208:211], v[74:81], v191
	s_waitcnt lgkmcnt(2)
	v_smfmac_f32_16x16x64_f16 v[200:203], v[212:215], v[50:57], v191
	v_smfmac_f32_16x16x64_f16 v[204:207], v[212:215], v[82:89], v191
	s_waitcnt lgkmcnt(1)
	v_smfmac_f32_16x16x64_f16 v[200:203], v[216:219], v[58:65], v191
	v_smfmac_f32_16x16x64_f16 v[204:207], v[216:219], v[90:97], v191
	s_waitcnt lgkmcnt(0)
	v_smfmac_f32_16x16x64_f16 v[200:203], v[220:223], v[66:73], v191
	v_smfmac_f32_16x16x64_f16 v[204:207], v[220:223], v[98:105], v191
	s_nop 6
	v_cndmask_b32_e64 v170, v201, v200, s[6:7]
	v_cndmask_b32_e64 v170, v170, v204, s[0:1]
	v_cndmask_b32_e64 v170, v170, v205, s[4:5]
	v_exp_f32_e32 v170, v170
	s_nop 0
	v_add_f32_e32 v170, 1.0, v170
	v_rcp_f32_e32 v170, v170
	s_nop 0
	v_fmac_f32_e32 v153, v170, v182
	s_nop 1
	v_add_f32_dpp v153, v153, v153 quad_perm:[1,0,3,2] row_mask:0xf bank_mask:0xf bound_ctrl:1
	s_nop 1
	v_add_f32_dpp v153, v153, v153 quad_perm:[2,3,0,1] row_mask:0xf bank_mask:0xf bound_ctrl:1
	s_nop 1
	v_add_f32_dpp v153, v153, v153 row_half_mirror row_mask:0xf bank_mask:0xf bound_ctrl:1
	v_cvt_f16_f32_e32 v170, v153
	ds_write_b16 v150, v170
	s_waitcnt lgkmcnt(0)
	s_barrier
	ds_read_b128 v[154:157], v147
	s_waitcnt lgkmcnt(0)
	v_smfmac_f32_16x16x64_f16 v[130:133], v[154:157], v[248:255], v191
	s_nop 2
	v_add_u32_e32 v134, s3, v151
	ds_read_b32 v135, v134
	s_nop 2
	v_cndmask_b32_e64 v136, v130, v131, s[0:1]
	v_exp_f32_e64 v158, -|v136|
	v_max_f32 v159, 0, v136
	v_add_f32 v158, 1.0, v158
	v_log_f32 v158, v158
	s_nop 0
	v_fma_mixlo_f16 v137, v158, 1.0, v159
	ds_write_b16 v148, v137
	v_mov_b32_e32 v192, v106
	v_mov_b32_e32 v193, v110
	v_add_f32_e32 v136, v152, v153
	v_mul_f32 v137, -2.0, v135
	s_nop 6
	ds_read_b128 v[208:211], v139
	s_waitcnt lgkmcnt(1)
	s_barrier
	ds_read_b128 v[212:215], v140
	ds_read_b128 v[216:219], v141
	s_waitcnt lgkmcnt(2)
	v_smfmac_f32_16x16x64_f16 v[192:195], v[208:211], v[6:13], v191
	ds_read_b128 v[220:223], v142
	s_waitcnt lgkmcnt(2)
	v_smfmac_f32_16x16x64_f16 v[192:195], v[212:215], v[14:21], v191
	s_waitcnt lgkmcnt(1)
	v_smfmac_f32_16x16x64_f16 v[192:195], v[216:219], v[26:33], v191
	s_waitcnt lgkmcnt(0)
	v_smfmac_f32_16x16x64_f16 v[192:195], v[220:223], v[34:41], v191
	s_nop 7
	v_cndmask_b32_e64 v152, v192, v193, s[0:1]
	v_exp_f32_e64 v158, -|v152|
	v_max_f32 v159, 0, v152
	v_add_f32 v158, 1.0, v158
	v_log_f32 v158, v158
	s_nop 0
	v_fma_mixlo_f16 v153, v158, 1.0, v159
	ds_write_b16 v149, v153
	v_mov_b32_e32 v200, v114
	v_mov_b32_e32 v201, v118
	v_mov_b32_e32 v204, v122
	v_mov_b32_e32 v205, v126
	s_nop 3
	ds_read_b128 v[208:211], v143
	s_waitcnt lgkmcnt(1)
	s_barrier
	ds_read_b128 v[212:215], v144
	ds_read_b128 v[216:219], v145
	s_waitcnt lgkmcnt(2)
	v_smfmac_f32_16x16x64_f16 v[200:203], v[208:211], v[42:49], v191
	ds_read_b128 v[220:223], v146
	v_smfmac_f32_16x16x64_f16 v[204:207], v[208:211], v[74:81], v191
	s_waitcnt lgkmcnt(2)
	v_smfmac_f32_16x16x64_f16 v[200:203], v[212:215], v[50:57], v191
	v_smfmac_f32_16x16x64_f16 v[204:207], v[212:215], v[82:89], v191
	s_waitcnt lgkmcnt(1)
	v_smfmac_f32_16x16x64_f16 v[200:203], v[216:219], v[58:65], v191
	v_smfmac_f32_16x16x64_f16 v[204:207], v[216:219], v[90:97], v191
	s_waitcnt lgkmcnt(0)
	v_smfmac_f32_16x16x64_f16 v[200:203], v[220:223], v[66:73], v191
	v_smfmac_f32_16x16x64_f16 v[204:207], v[220:223], v[98:105], v191
	s_nop 6
	v_cndmask_b32_e64 v152, v201, v200, s[6:7]
	v_cndmask_b32_e64 v152, v152, v204, s[0:1]
	v_cndmask_b32_e64 v152, v152, v205, s[4:5]
	v_exp_f32_e32 v152, v152
	s_nop 0
	v_add_f32_e32 v152, 1.0, v152
	v_rcp_f32_e32 v152, v152
	s_nop 0
	v_fmac_f32_e32 v135, v152, v137
	s_nop 1
	v_add_f32_dpp v135, v135, v135 quad_perm:[1,0,3,2] row_mask:0xf bank_mask:0xf bound_ctrl:1
	s_nop 1
	v_add_f32_dpp v135, v135, v135 quad_perm:[2,3,0,1] row_mask:0xf bank_mask:0xf bound_ctrl:1
	s_nop 1
	v_add_f32_dpp v135, v135, v135 row_half_mirror row_mask:0xf bank_mask:0xf bound_ctrl:1
	v_cvt_f16_f32_e32 v137, v135
	ds_write_b16 v150, v137
	s_waitcnt lgkmcnt(0)
	s_barrier
	ds_read_b128 v[158:161], v147
	ds_read_b32 v137, v134 offset:32
	v_add_f32_e32 v135, v136, v135
	s_waitcnt lgkmcnt(1)
	v_smfmac_f32_16x16x64_f16 v[130:133], v[158:161], v[248:255], v191
	s_nop 7
	v_cndmask_b32_e64 v156, v130, v131, s[0:1]
	v_exp_f32_e64 v158, -|v156|
	v_max_f32 v159, 0, v156
	v_add_f32 v158, 1.0, v158
	v_log_f32 v158, v158
	s_nop 0
	v_fma_mixlo_f16 v157, v158, 1.0, v159
	ds_write_b16 v148, v157
	v_mov_b32_e32 v192, v106
	v_mov_b32_e32 v193, v110
	v_mul_f32 v136, -2.0, v137
	s_nop 6
	ds_read_b128 v[208:211], v139
	s_waitcnt lgkmcnt(1)
	s_barrier
	ds_read_b128 v[212:215], v140
	ds_read_b128 v[216:219], v141
	s_waitcnt lgkmcnt(2)
	v_smfmac_f32_16x16x64_f16 v[192:195], v[208:211], v[6:13], v191
	ds_read_b128 v[220:223], v142
	s_waitcnt lgkmcnt(2)
	v_smfmac_f32_16x16x64_f16 v[192:195], v[212:215], v[14:21], v191
	s_waitcnt lgkmcnt(1)
	v_smfmac_f32_16x16x64_f16 v[192:195], v[216:219], v[26:33], v191
	s_waitcnt lgkmcnt(0)
	v_smfmac_f32_16x16x64_f16 v[192:195], v[220:223], v[34:41], v191
	s_nop 7
	v_cndmask_b32_e64 v156, v192, v193, s[0:1]
	v_exp_f32_e64 v158, -|v156|
	v_max_f32 v159, 0, v156
	v_add_f32 v158, 1.0, v158
	v_log_f32 v158, v158
	s_nop 0
	v_fma_mixlo_f16 v157, v158, 1.0, v159
	ds_write_b16 v149, v157
	v_mov_b32_e32 v200, v114
	v_mov_b32_e32 v201, v118
	v_mov_b32_e32 v204, v122
	v_mov_b32_e32 v205, v126
	s_nop 3
	ds_read_b128 v[208:211], v143
	s_waitcnt lgkmcnt(1)
	s_barrier
	ds_read_b128 v[212:215], v144
	ds_read_b128 v[216:219], v145
	s_waitcnt lgkmcnt(2)
	v_smfmac_f32_16x16x64_f16 v[200:203], v[208:211], v[42:49], v191
	ds_read_b128 v[220:223], v146
	v_smfmac_f32_16x16x64_f16 v[204:207], v[208:211], v[74:81], v191
	s_waitcnt lgkmcnt(2)
	v_smfmac_f32_16x16x64_f16 v[200:203], v[212:215], v[50:57], v191
	v_smfmac_f32_16x16x64_f16 v[204:207], v[212:215], v[82:89], v191
	s_waitcnt lgkmcnt(1)
	v_smfmac_f32_16x16x64_f16 v[200:203], v[216:219], v[58:65], v191
	v_smfmac_f32_16x16x64_f16 v[204:207], v[216:219], v[90:97], v191
	s_waitcnt lgkmcnt(0)
	v_smfmac_f32_16x16x64_f16 v[200:203], v[220:223], v[66:73], v191
	v_smfmac_f32_16x16x64_f16 v[204:207], v[220:223], v[98:105], v191
	s_nop 6
	v_cndmask_b32_e64 v172, v201, v200, s[6:7]
	v_cndmask_b32_e64 v172, v172, v204, s[0:1]
	v_cndmask_b32_e64 v172, v172, v205, s[4:5]
	v_exp_f32_e32 v172, v172
	s_nop 0
	v_add_f32_e32 v172, 1.0, v172
	v_rcp_f32_e32 v172, v172
	s_nop 0
	v_fmac_f32_e32 v137, v172, v136
	s_nop 1
	v_add_f32_dpp v136, v137, v137 quad_perm:[1,0,3,2] row_mask:0xf bank_mask:0xf bound_ctrl:1
	s_nop 1
	v_add_f32_dpp v136, v136, v136 quad_perm:[2,3,0,1] row_mask:0xf bank_mask:0xf bound_ctrl:1
	s_nop 1
	v_add_f32_dpp v136, v136, v136 row_half_mirror row_mask:0xf bank_mask:0xf bound_ctrl:1
	v_cvt_f16_f32_e32 v137, v136
	ds_write_b16 v150, v137
	s_waitcnt lgkmcnt(0)
	s_barrier
	ds_read_b128 v[156:159], v147
	ds_read_b32 v137, v134 offset:64
	v_add_f32_e32 v135, v135, v136
	s_waitcnt lgkmcnt(1)
	v_smfmac_f32_16x16x64_f16 v[130:133], v[156:159], v[248:255], v191
	s_nop 7
	v_cndmask_b32_e64 v156, v130, v131, s[0:1]
	v_exp_f32_e64 v158, -|v156|
	v_max_f32 v159, 0, v156
	v_add_f32 v158, 1.0, v158
	v_log_f32 v158, v158
	s_nop 0
	v_fma_mixlo_f16 v157, v158, 1.0, v159
	ds_write_b16 v148, v157
	v_mov_b32_e32 v192, v106
	v_mov_b32_e32 v193, v110
	v_mul_f32 v136, -2.0, v137
	s_nop 6
	ds_read_b128 v[208:211], v139
	s_waitcnt lgkmcnt(1)
	s_barrier
	ds_read_b128 v[212:215], v140
	ds_read_b128 v[216:219], v141
	s_waitcnt lgkmcnt(2)
	v_smfmac_f32_16x16x64_f16 v[192:195], v[208:211], v[6:13], v191
	ds_read_b128 v[220:223], v142
	s_waitcnt lgkmcnt(2)
	v_smfmac_f32_16x16x64_f16 v[192:195], v[212:215], v[14:21], v191
	s_waitcnt lgkmcnt(1)
	v_smfmac_f32_16x16x64_f16 v[192:195], v[216:219], v[26:33], v191
	s_waitcnt lgkmcnt(0)
	v_smfmac_f32_16x16x64_f16 v[192:195], v[220:223], v[34:41], v191
	s_nop 7
	v_cndmask_b32_e64 v156, v192, v193, s[0:1]
	v_exp_f32_e64 v158, -|v156|
	v_max_f32 v159, 0, v156
	v_add_f32 v158, 1.0, v158
	v_log_f32 v158, v158
	s_nop 0
	v_fma_mixlo_f16 v157, v158, 1.0, v159
	ds_write_b16 v149, v157
	v_mov_b32_e32 v200, v114
	v_mov_b32_e32 v201, v118
	v_mov_b32_e32 v204, v122
	v_mov_b32_e32 v205, v126
	s_nop 3
	ds_read_b128 v[208:211], v143
	s_waitcnt lgkmcnt(1)
	s_barrier
	ds_read_b128 v[212:215], v144
	ds_read_b128 v[216:219], v145
	s_waitcnt lgkmcnt(2)
	v_smfmac_f32_16x16x64_f16 v[200:203], v[208:211], v[42:49], v191
	ds_read_b128 v[220:223], v146
	v_smfmac_f32_16x16x64_f16 v[204:207], v[208:211], v[74:81], v191
	s_waitcnt lgkmcnt(2)
	v_smfmac_f32_16x16x64_f16 v[200:203], v[212:215], v[50:57], v191
	v_smfmac_f32_16x16x64_f16 v[204:207], v[212:215], v[82:89], v191
	s_waitcnt lgkmcnt(1)
	v_smfmac_f32_16x16x64_f16 v[200:203], v[216:219], v[58:65], v191
	v_smfmac_f32_16x16x64_f16 v[204:207], v[216:219], v[90:97], v191
	s_waitcnt lgkmcnt(0)
	v_smfmac_f32_16x16x64_f16 v[200:203], v[220:223], v[66:73], v191
	v_smfmac_f32_16x16x64_f16 v[204:207], v[220:223], v[98:105], v191
	s_nop 6
	v_cndmask_b32_e64 v172, v201, v200, s[6:7]
	v_cndmask_b32_e64 v172, v172, v204, s[0:1]
	v_cndmask_b32_e64 v172, v172, v205, s[4:5]
	v_exp_f32_e32 v172, v172
	s_nop 0
	v_add_f32_e32 v172, 1.0, v172
	v_rcp_f32_e32 v172, v172
	s_nop 0
	v_fmac_f32_e32 v137, v172, v136
	s_nop 1
	v_add_f32_dpp v136, v137, v137 quad_perm:[1,0,3,2] row_mask:0xf bank_mask:0xf bound_ctrl:1
	s_nop 1
	v_add_f32_dpp v136, v136, v136 quad_perm:[2,3,0,1] row_mask:0xf bank_mask:0xf bound_ctrl:1
	s_nop 1
	v_add_f32_dpp v136, v136, v136 row_half_mirror row_mask:0xf bank_mask:0xf bound_ctrl:1
	v_cvt_f16_f32_e32 v137, v136
	ds_write_b16 v150, v137
	s_waitcnt lgkmcnt(0)
	s_barrier
	ds_read_b128 v[156:159], v147
	ds_read_b32 v137, v134 offset:96
	v_add_f32_e32 v135, v135, v136
	s_waitcnt lgkmcnt(1)
	v_smfmac_f32_16x16x64_f16 v[130:133], v[156:159], v[248:255], v191
	s_nop 7
	v_cndmask_b32_e64 v156, v130, v131, s[0:1]
	v_exp_f32_e64 v158, -|v156|
	v_max_f32 v159, 0, v156
	v_add_f32 v158, 1.0, v158
	v_log_f32 v158, v158
	s_nop 0
	v_fma_mixlo_f16 v157, v158, 1.0, v159
	ds_write_b16 v148, v157
	v_mov_b32_e32 v192, v106
	v_mov_b32_e32 v193, v110
	v_mul_f32 v136, -2.0, v137
	s_nop 6
	ds_read_b128 v[208:211], v139
	s_waitcnt lgkmcnt(1)
	s_barrier
	ds_read_b128 v[212:215], v140
	ds_read_b128 v[216:219], v141
	s_waitcnt lgkmcnt(2)
	v_smfmac_f32_16x16x64_f16 v[192:195], v[208:211], v[6:13], v191
	ds_read_b128 v[220:223], v142
	s_waitcnt lgkmcnt(2)
	v_smfmac_f32_16x16x64_f16 v[192:195], v[212:215], v[14:21], v191
	s_waitcnt lgkmcnt(1)
	v_smfmac_f32_16x16x64_f16 v[192:195], v[216:219], v[26:33], v191
	s_waitcnt lgkmcnt(0)
	v_smfmac_f32_16x16x64_f16 v[192:195], v[220:223], v[34:41], v191
	s_nop 7
	v_cndmask_b32_e64 v156, v192, v193, s[0:1]
	v_exp_f32_e64 v158, -|v156|
	v_max_f32 v159, 0, v156
	v_add_f32 v158, 1.0, v158
	v_log_f32 v158, v158
	s_nop 0
	v_fma_mixlo_f16 v157, v158, 1.0, v159
	ds_write_b16 v149, v157
	v_mov_b32_e32 v200, v114
	v_mov_b32_e32 v201, v118
	v_mov_b32_e32 v204, v122
	v_mov_b32_e32 v205, v126
	s_nop 3
	ds_read_b128 v[208:211], v143
	s_waitcnt lgkmcnt(1)
	s_barrier
	ds_read_b128 v[212:215], v144
	ds_read_b128 v[216:219], v145
	s_waitcnt lgkmcnt(2)
	v_smfmac_f32_16x16x64_f16 v[200:203], v[208:211], v[42:49], v191
	ds_read_b128 v[220:223], v146
	v_smfmac_f32_16x16x64_f16 v[204:207], v[208:211], v[74:81], v191
	s_waitcnt lgkmcnt(2)
	v_smfmac_f32_16x16x64_f16 v[200:203], v[212:215], v[50:57], v191
	v_smfmac_f32_16x16x64_f16 v[204:207], v[212:215], v[82:89], v191
	s_waitcnt lgkmcnt(1)
	v_smfmac_f32_16x16x64_f16 v[200:203], v[216:219], v[58:65], v191
	v_smfmac_f32_16x16x64_f16 v[204:207], v[216:219], v[90:97], v191
	s_waitcnt lgkmcnt(0)
	v_smfmac_f32_16x16x64_f16 v[200:203], v[220:223], v[66:73], v191
	v_smfmac_f32_16x16x64_f16 v[204:207], v[220:223], v[98:105], v191
	s_nop 6
	v_cndmask_b32_e64 v172, v201, v200, s[6:7]
	v_cndmask_b32_e64 v172, v172, v204, s[0:1]
	v_cndmask_b32_e64 v172, v172, v205, s[4:5]
	v_exp_f32_e32 v172, v172
	s_nop 0
	v_add_f32_e32 v172, 1.0, v172
	v_rcp_f32_e32 v172, v172
	s_nop 0
	v_fmac_f32_e32 v137, v172, v136
	s_nop 1
	v_add_f32_dpp v136, v137, v137 quad_perm:[1,0,3,2] row_mask:0xf bank_mask:0xf bound_ctrl:1
	s_nop 1
	v_add_f32_dpp v136, v136, v136 quad_perm:[2,3,0,1] row_mask:0xf bank_mask:0xf bound_ctrl:1
	s_nop 1
	v_add_f32_dpp v136, v136, v136 row_half_mirror row_mask:0xf bank_mask:0xf bound_ctrl:1
	v_cvt_f16_f32_e32 v137, v136
	ds_write_b16 v150, v137
	s_waitcnt lgkmcnt(0)
	s_barrier
	ds_read_b128 v[156:159], v147
	ds_read_b32 v137, v134 offset:128
	v_add_f32_e32 v135, v135, v136
	s_waitcnt lgkmcnt(1)
	v_smfmac_f32_16x16x64_f16 v[130:133], v[156:159], v[248:255], v191
	s_nop 7
	v_cndmask_b32_e64 v156, v130, v131, s[0:1]
	v_exp_f32_e64 v158, -|v156|
	v_max_f32 v159, 0, v156
	v_add_f32 v158, 1.0, v158
	v_log_f32 v158, v158
	s_nop 0
	v_fma_mixlo_f16 v157, v158, 1.0, v159
	ds_write_b16 v148, v157
	v_mov_b32_e32 v192, v106
	v_mov_b32_e32 v193, v110
	v_mul_f32 v136, -2.0, v137
	s_nop 6
	ds_read_b128 v[208:211], v139
	s_waitcnt lgkmcnt(1)
	s_barrier
	ds_read_b128 v[212:215], v140
	ds_read_b128 v[216:219], v141
	s_waitcnt lgkmcnt(2)
	v_smfmac_f32_16x16x64_f16 v[192:195], v[208:211], v[6:13], v191
	ds_read_b128 v[220:223], v142
	s_waitcnt lgkmcnt(2)
	v_smfmac_f32_16x16x64_f16 v[192:195], v[212:215], v[14:21], v191
	s_waitcnt lgkmcnt(1)
	v_smfmac_f32_16x16x64_f16 v[192:195], v[216:219], v[26:33], v191
	s_waitcnt lgkmcnt(0)
	v_smfmac_f32_16x16x64_f16 v[192:195], v[220:223], v[34:41], v191
	s_nop 7
	v_cndmask_b32_e64 v156, v192, v193, s[0:1]
	v_exp_f32_e64 v158, -|v156|
	v_max_f32 v159, 0, v156
	v_add_f32 v158, 1.0, v158
	v_log_f32 v158, v158
	s_nop 0
	v_fma_mixlo_f16 v157, v158, 1.0, v159
	ds_write_b16 v149, v157
	v_mov_b32_e32 v200, v114
	v_mov_b32_e32 v201, v118
	v_mov_b32_e32 v204, v122
	v_mov_b32_e32 v205, v126
	s_nop 3
	ds_read_b128 v[208:211], v143
	s_waitcnt lgkmcnt(1)
	s_barrier
	ds_read_b128 v[212:215], v144
	ds_read_b128 v[216:219], v145
	s_waitcnt lgkmcnt(2)
	v_smfmac_f32_16x16x64_f16 v[200:203], v[208:211], v[42:49], v191
	ds_read_b128 v[220:223], v146
	v_smfmac_f32_16x16x64_f16 v[204:207], v[208:211], v[74:81], v191
	s_waitcnt lgkmcnt(2)
	v_smfmac_f32_16x16x64_f16 v[200:203], v[212:215], v[50:57], v191
	v_smfmac_f32_16x16x64_f16 v[204:207], v[212:215], v[82:89], v191
	s_waitcnt lgkmcnt(1)
	v_smfmac_f32_16x16x64_f16 v[200:203], v[216:219], v[58:65], v191
	v_smfmac_f32_16x16x64_f16 v[204:207], v[216:219], v[90:97], v191
	s_waitcnt lgkmcnt(0)
	v_smfmac_f32_16x16x64_f16 v[200:203], v[220:223], v[66:73], v191
	v_smfmac_f32_16x16x64_f16 v[204:207], v[220:223], v[98:105], v191
	s_nop 6
	v_cndmask_b32_e64 v172, v201, v200, s[6:7]
	v_cndmask_b32_e64 v172, v172, v204, s[0:1]
	v_cndmask_b32_e64 v172, v172, v205, s[4:5]
	v_exp_f32_e32 v172, v172
	s_nop 0
	v_add_f32_e32 v172, 1.0, v172
	v_rcp_f32_e32 v172, v172
	s_nop 0
	v_fmac_f32_e32 v137, v172, v136
	s_nop 1
	v_add_f32_dpp v136, v137, v137 quad_perm:[1,0,3,2] row_mask:0xf bank_mask:0xf bound_ctrl:1
	s_nop 1
	v_add_f32_dpp v136, v136, v136 quad_perm:[2,3,0,1] row_mask:0xf bank_mask:0xf bound_ctrl:1
	s_nop 1
	v_add_f32_dpp v136, v136, v136 row_half_mirror row_mask:0xf bank_mask:0xf bound_ctrl:1
	v_cvt_f16_f32_e32 v137, v136
	ds_write_b16 v150, v137
	s_waitcnt lgkmcnt(0)
	s_barrier
	ds_read_b128 v[156:159], v147
	ds_read_b32 v137, v134 offset:160
	v_add_f32_e32 v135, v135, v136
	s_waitcnt lgkmcnt(1)
	v_smfmac_f32_16x16x64_f16 v[130:133], v[156:159], v[248:255], v191
	s_nop 7
	v_cndmask_b32_e64 v156, v130, v131, s[0:1]
	v_exp_f32_e64 v158, -|v156|
	v_max_f32 v159, 0, v156
	v_add_f32 v158, 1.0, v158
	v_log_f32 v158, v158
	s_nop 0
	v_fma_mixlo_f16 v157, v158, 1.0, v159
	ds_write_b16 v148, v157
	v_mov_b32_e32 v192, v106
	v_mov_b32_e32 v193, v110
	v_mul_f32 v136, -2.0, v137
	s_nop 6
	ds_read_b128 v[208:211], v139
	s_waitcnt lgkmcnt(1)
	s_barrier
	ds_read_b128 v[212:215], v140
	ds_read_b128 v[216:219], v141
	s_waitcnt lgkmcnt(2)
	v_smfmac_f32_16x16x64_f16 v[192:195], v[208:211], v[6:13], v191
	ds_read_b128 v[220:223], v142
	s_waitcnt lgkmcnt(2)
	v_smfmac_f32_16x16x64_f16 v[192:195], v[212:215], v[14:21], v191
	s_waitcnt lgkmcnt(1)
	v_smfmac_f32_16x16x64_f16 v[192:195], v[216:219], v[26:33], v191
	s_waitcnt lgkmcnt(0)
	v_smfmac_f32_16x16x64_f16 v[192:195], v[220:223], v[34:41], v191
	s_nop 7
	v_cndmask_b32_e64 v156, v192, v193, s[0:1]
	v_exp_f32_e64 v158, -|v156|
	v_max_f32 v159, 0, v156
	v_add_f32 v158, 1.0, v158
	v_log_f32 v158, v158
	s_nop 0
	v_fma_mixlo_f16 v157, v158, 1.0, v159
	ds_write_b16 v149, v157
	v_mov_b32_e32 v200, v114
	v_mov_b32_e32 v201, v118
	v_mov_b32_e32 v204, v122
	v_mov_b32_e32 v205, v126
	s_nop 3
	ds_read_b128 v[208:211], v143
	s_waitcnt lgkmcnt(1)
	s_barrier
	ds_read_b128 v[212:215], v144
	ds_read_b128 v[216:219], v145
	s_waitcnt lgkmcnt(2)
	v_smfmac_f32_16x16x64_f16 v[200:203], v[208:211], v[42:49], v191
	ds_read_b128 v[220:223], v146
	v_smfmac_f32_16x16x64_f16 v[204:207], v[208:211], v[74:81], v191
	s_waitcnt lgkmcnt(2)
	v_smfmac_f32_16x16x64_f16 v[200:203], v[212:215], v[50:57], v191
	v_smfmac_f32_16x16x64_f16 v[204:207], v[212:215], v[82:89], v191
	s_waitcnt lgkmcnt(1)
	v_smfmac_f32_16x16x64_f16 v[200:203], v[216:219], v[58:65], v191
	v_smfmac_f32_16x16x64_f16 v[204:207], v[216:219], v[90:97], v191
	s_waitcnt lgkmcnt(0)
	v_smfmac_f32_16x16x64_f16 v[200:203], v[220:223], v[66:73], v191
	v_smfmac_f32_16x16x64_f16 v[204:207], v[220:223], v[98:105], v191
	s_nop 6
	v_cndmask_b32_e64 v172, v201, v200, s[6:7]
	v_cndmask_b32_e64 v172, v172, v204, s[0:1]
	v_cndmask_b32_e64 v172, v172, v205, s[4:5]
	v_exp_f32_e32 v172, v172
	s_nop 0
	v_add_f32_e32 v172, 1.0, v172
	v_rcp_f32_e32 v172, v172
	s_nop 0
	v_fmac_f32_e32 v137, v172, v136
	s_nop 1
	v_add_f32_dpp v136, v137, v137 quad_perm:[1,0,3,2] row_mask:0xf bank_mask:0xf bound_ctrl:1
	s_nop 1
	v_add_f32_dpp v136, v136, v136 quad_perm:[2,3,0,1] row_mask:0xf bank_mask:0xf bound_ctrl:1
	s_nop 1
	v_add_f32_dpp v136, v136, v136 row_half_mirror row_mask:0xf bank_mask:0xf bound_ctrl:1
	v_cvt_f16_f32_e32 v137, v136
	ds_write_b16 v150, v137
	s_waitcnt lgkmcnt(0)
	s_barrier
	ds_read_b128 v[156:159], v147
	ds_read_b32 v137, v134 offset:192
	v_add_f32_e32 v135, v135, v136
	s_waitcnt lgkmcnt(1)
	v_smfmac_f32_16x16x64_f16 v[130:133], v[156:159], v[248:255], v191
	s_nop 7
	v_cndmask_b32_e64 v152, v130, v131, s[0:1]
	v_exp_f32_e64 v158, -|v152|
	v_max_f32 v159, 0, v152
	v_add_f32 v158, 1.0, v158
	v_log_f32 v158, v158
	s_nop 0
	v_fma_mixlo_f16 v153, v158, 1.0, v159
	ds_write_b16 v148, v153
	v_mov_b32_e32 v192, v106
	v_mov_b32_e32 v193, v110
	v_mul_f32 v136, -2.0, v137
	s_nop 6
	ds_read_b128 v[208:211], v139
	s_waitcnt lgkmcnt(1)
	s_barrier
	ds_read_b128 v[212:215], v140
	ds_read_b128 v[216:219], v141
	s_waitcnt lgkmcnt(2)
	v_smfmac_f32_16x16x64_f16 v[192:195], v[208:211], v[6:13], v191
	ds_read_b128 v[220:223], v142
	s_waitcnt lgkmcnt(2)
	v_smfmac_f32_16x16x64_f16 v[192:195], v[212:215], v[14:21], v191
	s_waitcnt lgkmcnt(1)
	v_smfmac_f32_16x16x64_f16 v[192:195], v[216:219], v[26:33], v191
	s_waitcnt lgkmcnt(0)
	v_smfmac_f32_16x16x64_f16 v[192:195], v[220:223], v[34:41], v191
	s_nop 7
	v_cndmask_b32_e64 v152, v192, v193, s[0:1]
	v_exp_f32_e64 v158, -|v152|
	v_max_f32 v159, 0, v152
	v_add_f32 v158, 1.0, v158
	v_log_f32 v158, v158
	s_nop 0
	v_fma_mixlo_f16 v153, v158, 1.0, v159
	ds_write_b16 v149, v153
	v_mov_b32_e32 v200, v114
	v_mov_b32_e32 v201, v118
	v_mov_b32_e32 v204, v122
	v_mov_b32_e32 v205, v126
	s_nop 3
	ds_read_b128 v[208:211], v143
	s_waitcnt lgkmcnt(1)
	s_barrier
	ds_read_b128 v[212:215], v144
	ds_read_b128 v[216:219], v145
	s_waitcnt lgkmcnt(2)
	v_smfmac_f32_16x16x64_f16 v[200:203], v[208:211], v[42:49], v191
	ds_read_b128 v[220:223], v146
	v_smfmac_f32_16x16x64_f16 v[204:207], v[208:211], v[74:81], v191
	s_waitcnt lgkmcnt(2)
	v_smfmac_f32_16x16x64_f16 v[200:203], v[212:215], v[50:57], v191
	v_smfmac_f32_16x16x64_f16 v[204:207], v[212:215], v[82:89], v191
	s_waitcnt lgkmcnt(1)
	v_smfmac_f32_16x16x64_f16 v[200:203], v[216:219], v[58:65], v191
	v_smfmac_f32_16x16x64_f16 v[204:207], v[216:219], v[90:97], v191
	s_waitcnt lgkmcnt(0)
	v_smfmac_f32_16x16x64_f16 v[200:203], v[220:223], v[66:73], v191
	v_smfmac_f32_16x16x64_f16 v[204:207], v[220:223], v[98:105], v191
	s_nop 6
	v_cndmask_b32_e64 v152, v201, v200, s[6:7]
	v_cndmask_b32_e64 v152, v152, v204, s[0:1]
	v_cndmask_b32_e64 v152, v152, v205, s[4:5]
	v_exp_f32_e32 v152, v152
	s_nop 0
	v_add_f32_e32 v152, 1.0, v152
	v_rcp_f32_e32 v152, v152
	s_nop 0
	v_fmac_f32_e32 v137, v152, v136
	s_nop 1
	v_add_f32_dpp v136, v137, v137 quad_perm:[1,0,3,2] row_mask:0xf bank_mask:0xf bound_ctrl:1
	s_nop 1
	v_add_f32_dpp v136, v136, v136 quad_perm:[2,3,0,1] row_mask:0xf bank_mask:0xf bound_ctrl:1
	s_nop 1
	v_add_f32_dpp v136, v136, v136 row_half_mirror row_mask:0xf bank_mask:0xf bound_ctrl:1
	v_cvt_f16_f32_e32 v137, v136
	ds_write_b16 v150, v137
	s_waitcnt lgkmcnt(0)
	s_barrier
	ds_read_b128 v[158:161], v147
	v_add_f32_e32 v152, v135, v136
	ds_read_b32 v153, v134 offset:224
	s_addk_i32 s3, 0x100
	s_cmpk_eq_u32 s3, 0xfa20
	s_waitcnt lgkmcnt(1)
	v_smfmac_f32_16x16x64_f16 v[130:133], v[158:161], v[248:255], v191
	s_nop 7
	v_cndmask_b32_e64 v154, v130, v131, s[0:1]
	s_cbranch_scc0 .LBB0_21
	s_and_saveexec_b64 s[0:1], vcc
	ds_write_b32 v1, v152
	s_or_b64 exec, exec, s[0:1]
	v_cmp_gt_u32_e32 vcc, 10, v0
	s_waitcnt lgkmcnt(0)
	s_barrier
	s_and_saveexec_b64 s[0:1], vcc
	s_cbranch_execz .LBB0_28
	v_lshlrev_b32_e32 v1, 2, v0
	global_load_dword v1, v1, s[12:13]
	v_mov_b32_e32 v139, 0
	v_lshl_add_u64 v[2:3], s[10:11], 0, v[138:139]
	v_lshl_add_u64 v[2:3], v[2:3], 0, 28
	s_mov_b32 s0, 0
